# segment-edge trimming extended to all seven GEMM K-loops (closing barrier right after last MFMA, setprio 1 before opening barrier, single lgkmcnt wait)
# baseline (speedup 1.0000x reference)
.LBB0_424:
	s_add_u32 s12, s10, 0x3200
	s_addc_u32 s13, s11, 0
	s_add_i32 s38, 0, 0x10000
	v_add_u32_e32 v147, s38, v145
	ds_read_b128 v[148:151], v147
	ds_read_b128 v[152:155], v147 offset:1024
	ds_read_b128 v[156:159], v147 offset:2048
	ds_read_b128 v[160:163], v147 offset:3072
	s_cmp_eq_u32 s37, 12
	s_cselect_b32 s17, s5, s13
	s_cselect_b32 s16, s4, s12
	s_cselect_b32 s15, s7, s36
	s_cselect_b32 s14, s6, s35
	v_lshl_add_u64 v[184:185], s[10:11], 0, v[142:143]
	s_add_i32 m0, s24, 0xc000
	ds_read_b128 v[164:167], v146
	ds_read_b128 v[172:175], v146 offset:1024
	ds_read_b128 v[176:179], v146 offset:2048
	ds_read_b128 v[180:183], v146 offset:3072
	ds_read_b128 v[208:211], v146 offset:4096
	ds_read_b128 v[212:215], v146 offset:5120
	ds_read_b128 v[216:219], v146 offset:6144
	ds_read_b128 v[220:223], v146 offset:7168
	global_load_lds_dwordx4 v[184:185], off
	v_lshl_add_u64 v[184:185], s[10:11], 0, v[140:141]
	s_add_i32 m0, s24, 0xe000
	s_nop 0
	global_load_lds_dwordx4 v[184:185], off
	s_waitcnt lgkmcnt(8)
	s_setprio 1
	s_barrier
	s_waitcnt lgkmcnt(0)
	v_mfma_f32_16x16x32_bf16 v[124:127], v[148:151], v[164:167], v[124:127]
	v_mfma_f32_16x16x32_bf16 v[104:107], v[156:159], v[164:167], v[104:107]
	v_mfma_f32_16x16x32_bf16 v[120:123], v[148:151], v[176:179], v[120:123]
	v_mfma_f32_16x16x32_bf16 v[92:95], v[156:159], v[176:179], v[92:95]
	v_mfma_f32_16x16x32_bf16 v[116:119], v[148:151], v[208:211], v[116:119]
	v_mfma_f32_16x16x32_bf16 v[84:87], v[156:159], v[208:211], v[84:87]
	v_mfma_f32_16x16x32_bf16 v[112:115], v[148:151], v[216:219], v[112:115]
	v_mfma_f32_16x16x32_bf16 v[80:83], v[156:159], v[216:219], v[80:83]
	v_mfma_f32_16x16x32_bf16 v[124:127], v[152:155], v[172:175], v[124:127]
	v_mfma_f32_16x16x32_bf16 v[104:107], v[160:163], v[172:175], v[104:107]
	v_mfma_f32_16x16x32_bf16 v[120:123], v[152:155], v[180:183], v[120:123]
	v_mfma_f32_16x16x32_bf16 v[92:95], v[160:163], v[180:183], v[92:95]
	v_mfma_f32_16x16x32_bf16 v[116:119], v[152:155], v[212:215], v[116:119]
	v_mfma_f32_16x16x32_bf16 v[84:87], v[160:163], v[212:215], v[84:87]
	v_mfma_f32_16x16x32_bf16 v[112:115], v[152:155], v[220:223], v[112:115]
	v_mfma_f32_16x16x32_bf16 v[80:83], v[160:163], v[220:223], v[80:83]
	s_barrier
	s_setprio 0
	s_add_i32 s39, 0, 0x14000
	s_add_i32 s10, s38, s23
	v_add_u32_e32 v147, s39, v145
	v_lshl_add_u64 v[184:185], s[14:15], 0, v[168:169]
	s_mov_b32 m0, s10
	ds_read_b128 v[224:227], v147
	ds_read_b128 v[228:231], v147 offset:1024
	ds_read_b128 v[232:235], v147 offset:2048
	ds_read_b128 v[236:239], v147 offset:3072
	global_load_lds_dwordx4 v[184:185], off
	v_lshl_add_u64 v[240:241], s[14:15], 0, v[132:133]
	s_add_i32 m0, s10, 0x2000
	s_nop 0
	global_load_lds_dwordx4 v[240:241], off
	s_setprio 1
	s_barrier
	s_waitcnt lgkmcnt(0)
	v_mfma_f32_16x16x32_bf16 v[76:79], v[224:227], v[164:167], v[76:79]
	v_mfma_f32_16x16x32_bf16 v[64:67], v[232:235], v[164:167], v[64:67]
	v_mfma_f32_16x16x32_bf16 v[68:71], v[224:227], v[176:179], v[68:71]
	v_mfma_f32_16x16x32_bf16 v[52:55], v[232:235], v[176:179], v[52:55]
	v_mfma_f32_16x16x32_bf16 v[56:59], v[224:227], v[208:211], v[56:59]
	v_mfma_f32_16x16x32_bf16 v[44:47], v[232:235], v[208:211], v[44:47]
	v_mfma_f32_16x16x32_bf16 v[48:51], v[224:227], v[216:219], v[48:51]
	v_mfma_f32_16x16x32_bf16 v[32:35], v[232:235], v[216:219], v[32:35]
	v_mfma_f32_16x16x32_bf16 v[76:79], v[228:231], v[172:175], v[76:79]
	v_mfma_f32_16x16x32_bf16 v[64:67], v[236:239], v[172:175], v[64:67]
	v_mfma_f32_16x16x32_bf16 v[68:71], v[228:231], v[180:183], v[68:71]
	v_mfma_f32_16x16x32_bf16 v[52:55], v[236:239], v[180:183], v[52:55]
	v_mfma_f32_16x16x32_bf16 v[56:59], v[228:231], v[212:215], v[56:59]
	v_mfma_f32_16x16x32_bf16 v[44:47], v[236:239], v[212:215], v[44:47]
	v_mfma_f32_16x16x32_bf16 v[48:51], v[228:231], v[220:223], v[48:51]
	v_mfma_f32_16x16x32_bf16 v[32:35], v[236:239], v[220:223], v[32:35]
	s_barrier
	s_setprio 0
	s_mov_b32 m0, s24
	v_lshl_add_u64 v[242:243], s[16:17], 0, v[134:135]
	ds_read_b128 v[164:167], v146 offset:16384
	ds_read_b128 v[172:175], v146 offset:17408
	ds_read_b128 v[176:179], v146 offset:18432
	ds_read_b128 v[180:183], v146 offset:19456
	ds_read_b128 v[208:211], v146 offset:20480
	ds_read_b128 v[212:215], v146 offset:21504
	ds_read_b128 v[216:219], v146 offset:22528
	ds_read_b128 v[220:223], v146 offset:23552
	global_load_lds_dwordx4 v[242:243], off
	v_lshl_add_u64 v[244:245], s[16:17], 0, v[128:129]
	s_mov_b32 m0, s25
	s_nop 0
	global_load_lds_dwordx4 v[244:245], off
	s_setprio 1
	s_barrier
	s_waitcnt lgkmcnt(0)
	v_mfma_f32_16x16x32_bf16 v[72:75], v[148:151], v[164:167], v[72:75]
	v_mfma_f32_16x16x32_bf16 v[40:43], v[156:159], v[164:167], v[40:43]
	v_mfma_f32_16x16x32_bf16 v[60:63], v[148:151], v[176:179], v[60:63]
	v_mfma_f32_16x16x32_bf16 v[28:31], v[156:159], v[176:179], v[28:31]
	v_mfma_f32_16x16x32_bf16 v[36:39], v[148:151], v[208:211], v[36:39]
	v_mfma_f32_16x16x32_bf16 v[20:23], v[156:159], v[208:211], v[20:23]
	v_mfma_f32_16x16x32_bf16 v[24:27], v[148:151], v[216:219], v[24:27]
	v_mfma_f32_16x16x32_bf16 v[16:19], v[156:159], v[216:219], v[16:19]
	v_mfma_f32_16x16x32_bf16 v[72:75], v[152:155], v[172:175], v[72:75]
	v_mfma_f32_16x16x32_bf16 v[40:43], v[160:163], v[172:175], v[40:43]
	v_mfma_f32_16x16x32_bf16 v[60:63], v[152:155], v[180:183], v[60:63]
	v_mfma_f32_16x16x32_bf16 v[28:31], v[160:163], v[180:183], v[28:31]
	v_mfma_f32_16x16x32_bf16 v[36:39], v[152:155], v[212:215], v[36:39]
	v_mfma_f32_16x16x32_bf16 v[20:23], v[160:163], v[212:215], v[20:23]
	v_mfma_f32_16x16x32_bf16 v[24:27], v[152:155], v[220:223], v[24:27]
	v_mfma_f32_16x16x32_bf16 v[16:19], v[160:163], v[220:223], v[16:19]
	s_barrier
	s_setprio 0
	s_add_u32 s10, s14, 0x100000
	s_addc_u32 s11, s15, 0
	s_add_i32 s38, s39, s23
	v_lshl_add_u64 v[148:149], s[10:11], 0, v[168:169]
	s_mov_b32 m0, s38
	s_nop 0
	global_load_lds_dwordx4 v[148:149], off
	v_lshl_add_u64 v[148:149], s[10:11], 0, v[132:133]
	s_add_i32 m0, s38, 0x2000
	s_nop 0
	global_load_lds_dwordx4 v[148:149], off
	s_waitcnt vmcnt(6)
	s_setprio 1
	s_barrier
	v_mfma_f32_16x16x32_bf16 v[12:15], v[224:227], v[164:167], v[12:15]
	v_mfma_f32_16x16x32_bf16 v[4:7], v[232:235], v[164:167], v[4:7]
	v_mfma_f32_16x16x32_bf16 v[8:11], v[224:227], v[176:179], v[8:11]
	v_mfma_f32_16x16x32_bf16 v[0:3], v[232:235], v[176:179], v[0:3]
	v_mfma_f32_16x16x32_bf16 v[96:99], v[224:227], v[208:211], v[96:99]
	v_mfma_f32_16x16x32_bf16 v[88:91], v[232:235], v[208:211], v[88:91]
	v_mfma_f32_16x16x32_bf16 v[108:111], v[224:227], v[216:219], v[108:111]
	v_mfma_f32_16x16x32_bf16 v[100:103], v[232:235], v[216:219], v[100:103]
	v_mfma_f32_16x16x32_bf16 v[12:15], v[228:231], v[172:175], v[12:15]
	v_mfma_f32_16x16x32_bf16 v[4:7], v[236:239], v[172:175], v[4:7]
	v_mfma_f32_16x16x32_bf16 v[8:11], v[228:231], v[180:183], v[8:11]
	v_mfma_f32_16x16x32_bf16 v[0:3], v[236:239], v[180:183], v[0:3]
	v_mfma_f32_16x16x32_bf16 v[96:99], v[228:231], v[212:215], v[96:99]
	v_mfma_f32_16x16x32_bf16 v[88:91], v[236:239], v[212:215], v[88:91]
	v_mfma_f32_16x16x32_bf16 v[108:111], v[228:231], v[220:223], v[108:111]
	v_mfma_f32_16x16x32_bf16 v[100:103], v[236:239], v[220:223], v[100:103]
	s_barrier
	s_setprio 0
	s_add_i32 s10, 0, 0x18000
	v_add_u32_e32 v147, s10, v145
	ds_read_b128 v[148:151], v147
	ds_read_b128 v[152:155], v147 offset:1024
	ds_read_b128 v[156:159], v147 offset:2048
	ds_read_b128 v[160:163], v147 offset:3072
	s_mov_b32 m0, s26
	v_lshl_add_u64 v[224:225], s[16:17], 0, v[136:137]
	ds_read_b128 v[164:167], v146 offset:32768
	ds_read_b128 v[172:175], v146 offset:33792
	ds_read_b128 v[176:179], v146 offset:34816
	ds_read_b128 v[180:183], v146 offset:35840
	ds_read_b128 v[208:211], v146 offset:36864
	ds_read_b128 v[212:215], v146 offset:37888
	ds_read_b128 v[216:219], v146 offset:38912
	ds_read_b128 v[220:223], v146 offset:39936
	global_load_lds_dwordx4 v[224:225], off
	v_lshl_add_u64 v[224:225], s[16:17], 0, v[130:131]
	s_mov_b32 m0, s27
	s_nop 0
	global_load_lds_dwordx4 v[224:225], off
	s_waitcnt lgkmcnt(8)
	s_setprio 1
	s_barrier
	s_waitcnt lgkmcnt(0)
	v_mfma_f32_16x16x32_bf16 v[124:127], v[148:151], v[164:167], v[124:127]
	v_mfma_f32_16x16x32_bf16 v[104:107], v[156:159], v[164:167], v[104:107]
	v_mfma_f32_16x16x32_bf16 v[120:123], v[148:151], v[176:179], v[120:123]
	v_mfma_f32_16x16x32_bf16 v[92:95], v[156:159], v[176:179], v[92:95]
	v_mfma_f32_16x16x32_bf16 v[116:119], v[148:151], v[208:211], v[116:119]
	v_mfma_f32_16x16x32_bf16 v[84:87], v[156:159], v[208:211], v[84:87]
	v_mfma_f32_16x16x32_bf16 v[112:115], v[148:151], v[216:219], v[112:115]
	v_mfma_f32_16x16x32_bf16 v[80:83], v[156:159], v[216:219], v[80:83]
	v_mfma_f32_16x16x32_bf16 v[124:127], v[152:155], v[172:175], v[124:127]
	v_mfma_f32_16x16x32_bf16 v[104:107], v[160:163], v[172:175], v[104:107]
	v_mfma_f32_16x16x32_bf16 v[120:123], v[152:155], v[180:183], v[120:123]
	v_mfma_f32_16x16x32_bf16 v[92:95], v[160:163], v[180:183], v[92:95]
	v_mfma_f32_16x16x32_bf16 v[116:119], v[152:155], v[212:215], v[116:119]
	v_mfma_f32_16x16x32_bf16 v[84:87], v[160:163], v[212:215], v[84:87]
	v_mfma_f32_16x16x32_bf16 v[112:115], v[152:155], v[220:223], v[112:115]
	v_mfma_f32_16x16x32_bf16 v[80:83], v[160:163], v[220:223], v[80:83]
	s_barrier
	s_setprio 0
	s_add_i32 s16, 0, 0x1c000
	s_add_i32 s10, s10, s23
	v_add_u32_e32 v147, s16, v145
	v_lshl_add_u64 v[184:185], v[184:185], 0, s[94:95]
	s_mov_b32 m0, s10
	ds_read_b128 v[224:227], v147
	ds_read_b128 v[228:231], v147 offset:1024
	ds_read_b128 v[232:235], v147 offset:2048
	ds_read_b128 v[236:239], v147 offset:3072
	global_load_lds_dwordx4 v[184:185], off
	v_lshl_add_u64 v[184:185], v[240:241], 0, s[94:95]
	s_add_i32 m0, s10, 0x2000
	s_nop 0
	global_load_lds_dwordx4 v[184:185], off
	s_setprio 1
	s_barrier
	s_waitcnt lgkmcnt(0)
	v_mfma_f32_16x16x32_bf16 v[76:79], v[224:227], v[164:167], v[76:79]
	v_mfma_f32_16x16x32_bf16 v[64:67], v[232:235], v[164:167], v[64:67]
	v_mfma_f32_16x16x32_bf16 v[68:71], v[224:227], v[176:179], v[68:71]
	v_mfma_f32_16x16x32_bf16 v[52:55], v[232:235], v[176:179], v[52:55]
	v_mfma_f32_16x16x32_bf16 v[56:59], v[224:227], v[208:211], v[56:59]
	v_mfma_f32_16x16x32_bf16 v[44:47], v[232:235], v[208:211], v[44:47]
	v_mfma_f32_16x16x32_bf16 v[48:51], v[224:227], v[216:219], v[48:51]
	v_mfma_f32_16x16x32_bf16 v[32:35], v[232:235], v[216:219], v[32:35]
	v_mfma_f32_16x16x32_bf16 v[76:79], v[228:231], v[172:175], v[76:79]
	v_mfma_f32_16x16x32_bf16 v[64:67], v[236:239], v[172:175], v[64:67]
	v_mfma_f32_16x16x32_bf16 v[68:71], v[228:231], v[180:183], v[68:71]
	v_mfma_f32_16x16x32_bf16 v[52:55], v[236:239], v[180:183], v[52:55]
	v_mfma_f32_16x16x32_bf16 v[56:59], v[228:231], v[212:215], v[56:59]
	v_mfma_f32_16x16x32_bf16 v[44:47], v[236:239], v[212:215], v[44:47]
	v_mfma_f32_16x16x32_bf16 v[48:51], v[228:231], v[220:223], v[48:51]
	v_mfma_f32_16x16x32_bf16 v[32:35], v[236:239], v[220:223], v[32:35]
	s_barrier
	s_setprio 0
	s_mov_b32 m0, s28
	v_lshl_add_u64 v[184:185], v[242:243], 0, s[94:95]
	ds_read_b128 v[164:167], v146 offset:49152
	ds_read_b128 v[172:175], v146 offset:50176
	ds_read_b128 v[176:179], v146 offset:51200
	ds_read_b128 v[180:183], v146 offset:52224
	ds_read_b128 v[208:211], v146 offset:53248
	ds_read_b128 v[212:215], v146 offset:54272
	ds_read_b128 v[216:219], v146 offset:55296
	ds_read_b128 v[220:223], v146 offset:56320
	global_load_lds_dwordx4 v[184:185], off
	v_lshl_add_u64 v[184:185], v[244:245], 0, s[94:95]
	s_mov_b32 m0, s29
	s_nop 0
	global_load_lds_dwordx4 v[184:185], off
	s_setprio 1
	s_barrier
	s_waitcnt lgkmcnt(0)
	v_mfma_f32_16x16x32_bf16 v[72:75], v[148:151], v[164:167], v[72:75]
	v_mfma_f32_16x16x32_bf16 v[40:43], v[156:159], v[164:167], v[40:43]
	v_mfma_f32_16x16x32_bf16 v[60:63], v[148:151], v[176:179], v[60:63]
	v_mfma_f32_16x16x32_bf16 v[28:31], v[156:159], v[176:179], v[28:31]
	v_mfma_f32_16x16x32_bf16 v[36:39], v[148:151], v[208:211], v[36:39]
	v_mfma_f32_16x16x32_bf16 v[20:23], v[156:159], v[208:211], v[20:23]
	v_mfma_f32_16x16x32_bf16 v[24:27], v[148:151], v[216:219], v[24:27]
	v_mfma_f32_16x16x32_bf16 v[16:19], v[156:159], v[216:219], v[16:19]
	v_mfma_f32_16x16x32_bf16 v[72:75], v[152:155], v[172:175], v[72:75]
	v_mfma_f32_16x16x32_bf16 v[40:43], v[160:163], v[172:175], v[40:43]
	v_mfma_f32_16x16x32_bf16 v[60:63], v[152:155], v[180:183], v[60:63]
	v_mfma_f32_16x16x32_bf16 v[28:31], v[160:163], v[180:183], v[28:31]
	v_mfma_f32_16x16x32_bf16 v[36:39], v[152:155], v[212:215], v[36:39]
	v_mfma_f32_16x16x32_bf16 v[20:23], v[160:163], v[212:215], v[20:23]
	v_mfma_f32_16x16x32_bf16 v[24:27], v[152:155], v[220:223], v[24:27]
	v_mfma_f32_16x16x32_bf16 v[16:19], v[160:163], v[220:223], v[16:19]
	s_barrier
	s_setprio 0
	s_add_u32 s10, s14, 0x100080
	s_addc_u32 s11, s15, 0
	s_add_i32 s14, s16, s23
	v_lshl_add_u64 v[148:149], s[10:11], 0, v[168:169]
	s_mov_b32 m0, s14
	s_nop 0
	global_load_lds_dwordx4 v[148:149], off
	v_lshl_add_u64 v[148:149], s[10:11], 0, v[132:133]
	s_add_i32 m0, s14, 0x2000
	s_nop 0
	global_load_lds_dwordx4 v[148:149], off
	s_waitcnt vmcnt(6)
	s_setprio 1
	s_barrier
	v_mfma_f32_16x16x32_bf16 v[12:15], v[224:227], v[164:167], v[12:15]
	v_mfma_f32_16x16x32_bf16 v[4:7], v[232:235], v[164:167], v[4:7]
	v_mfma_f32_16x16x32_bf16 v[8:11], v[224:227], v[176:179], v[8:11]
	v_mfma_f32_16x16x32_bf16 v[0:3], v[232:235], v[176:179], v[0:3]
	v_mfma_f32_16x16x32_bf16 v[96:99], v[224:227], v[208:211], v[96:99]
	v_mfma_f32_16x16x32_bf16 v[88:91], v[232:235], v[208:211], v[88:91]
	v_mfma_f32_16x16x32_bf16 v[108:111], v[224:227], v[216:219], v[108:111]
	v_mfma_f32_16x16x32_bf16 v[100:103], v[232:235], v[216:219], v[100:103]
	v_mfma_f32_16x16x32_bf16 v[12:15], v[228:231], v[172:175], v[12:15]
	v_mfma_f32_16x16x32_bf16 v[4:7], v[236:239], v[172:175], v[4:7]
	v_mfma_f32_16x16x32_bf16 v[8:11], v[228:231], v[180:183], v[8:11]
	v_mfma_f32_16x16x32_bf16 v[0:3], v[236:239], v[180:183], v[0:3]
	v_mfma_f32_16x16x32_bf16 v[96:99], v[228:231], v[212:215], v[96:99]
	v_mfma_f32_16x16x32_bf16 v[88:91], v[236:239], v[212:215], v[88:91]
	v_mfma_f32_16x16x32_bf16 v[108:111], v[228:231], v[220:223], v[108:111]
	v_mfma_f32_16x16x32_bf16 v[100:103], v[236:239], v[220:223], v[100:103]
	s_barrier
	s_setprio 0
	s_add_i32 s37, s37, 2
	s_add_u32 s35, s35, 0x100
	s_addc_u32 s36, s36, 0
	s_cmp_gt_u32 s37, 13
	s_mov_b64 s[10:11], s[12:13]
	s_cbranch_scc0 .LBB0_424
	s_and_b64 vcc, exec, s[2:3]
	s_cbranch_vccz .LBB0_427
	s_barrier

.LBB0_440:
	s_add_u32 s14, s12, 0x80
	s_addc_u32 s15, s13, 0
	s_add_i32 s42, 0, 0x10000
	v_add_u32_e32 v79, s42, v77
	ds_read_b128 v[80:83], v79
	ds_read_b128 v[84:87], v79 offset:1024
	ds_read_b128 v[88:91], v79 offset:2048
	ds_read_b128 v[92:95], v79 offset:3072
	s_cmp_eq_u32 s41, 12
	s_cselect_b32 s17, s7, s15
	s_cselect_b32 s16, s6, s14
	s_cselect_b32 s15, s9, s40
	s_cselect_b32 s14, s8, s39
	v_lshl_add_u64 v[128:129], s[12:13], 0, v[74:75]
	s_add_i32 m0, s24, 0xc000
	ds_read_b128 v[96:99], v78
	ds_read_b128 v[100:103], v78 offset:1024
	ds_read_b128 v[104:107], v78 offset:2048
	ds_read_b128 v[108:111], v78 offset:3072
	ds_read_b128 v[112:115], v78 offset:4096
	ds_read_b128 v[116:119], v78 offset:5120
	ds_read_b128 v[120:123], v78 offset:6144
	ds_read_b128 v[124:127], v78 offset:7168
	global_load_lds_dwordx4 v[128:129], off
	v_lshl_add_u64 v[128:129], s[12:13], 0, v[72:73]
	s_add_i32 m0, s24, 0xe000
	s_nop 0
	global_load_lds_dwordx4 v[128:129], off
	s_waitcnt lgkmcnt(8)
	s_setprio 1
	s_barrier
	s_waitcnt lgkmcnt(0)
	v_mfma_f32_16x16x32_bf16 v[60:63], v[80:83], v[96:99], v[60:63]
	v_mfma_f32_16x16x32_bf16 v[44:47], v[88:91], v[96:99], v[44:47]
	v_mfma_f32_16x16x32_bf16 v[56:59], v[80:83], v[104:107], v[56:59]
	v_mfma_f32_16x16x32_bf16 v[36:39], v[88:91], v[104:107], v[36:39]
	v_mfma_f32_16x16x32_bf16 v[52:55], v[80:83], v[112:115], v[52:55]
	v_mfma_f32_16x16x32_bf16 v[32:35], v[88:91], v[112:115], v[32:35]
	v_mfma_f32_16x16x32_bf16 v[48:51], v[80:83], v[120:123], v[48:51]
	v_mfma_f32_16x16x32_bf16 v[24:27], v[88:91], v[120:123], v[24:27]
	v_mfma_f32_16x16x32_bf16 v[60:63], v[84:87], v[100:103], v[60:63]
	v_mfma_f32_16x16x32_bf16 v[44:47], v[92:95], v[100:103], v[44:47]
	v_mfma_f32_16x16x32_bf16 v[56:59], v[84:87], v[108:111], v[56:59]
	v_mfma_f32_16x16x32_bf16 v[36:39], v[92:95], v[108:111], v[36:39]
	v_mfma_f32_16x16x32_bf16 v[52:55], v[84:87], v[116:119], v[52:55]
	v_mfma_f32_16x16x32_bf16 v[32:35], v[92:95], v[116:119], v[32:35]
	v_mfma_f32_16x16x32_bf16 v[48:51], v[84:87], v[124:127], v[48:51]
	v_mfma_f32_16x16x32_bf16 v[24:27], v[92:95], v[124:127], v[24:27]
	s_barrier
	s_setprio 0
	s_add_i32 s42, s42, s23
	v_lshl_add_u64 v[128:129], s[14:15], 0, v[168:169]
	s_mov_b32 m0, s42
	v_lshl_add_u64 v[130:131], s[14:15], 0, v[64:65]
	global_load_lds_dwordx4 v[128:129], off
	s_add_i32 m0, s42, 0x2000
	s_nop 0
	global_load_lds_dwordx4 v[130:131], off
	s_barrier
	s_waitcnt lgkmcnt(0)
	s_setprio 1
	s_setprio 0
	s_mov_b32 m0, s24
	v_lshl_add_u64 v[132:133], s[16:17], 0, v[168:169]
	s_barrier
	ds_read_b128 v[96:99], v78 offset:16384
	ds_read_b128 v[100:103], v78 offset:17408
	ds_read_b128 v[104:107], v78 offset:18432
	ds_read_b128 v[108:111], v78 offset:19456
	ds_read_b128 v[112:115], v78 offset:20480
	ds_read_b128 v[116:119], v78 offset:21504
	ds_read_b128 v[120:123], v78 offset:22528
	ds_read_b128 v[124:127], v78 offset:23552
	global_load_lds_dwordx4 v[132:133], off
	v_lshl_add_u64 v[134:135], s[16:17], 0, v[64:65]
	s_mov_b32 m0, s25
	s_nop 0
	global_load_lds_dwordx4 v[134:135], off
	s_setprio 1
	s_barrier
	s_waitcnt lgkmcnt(0)
	v_mfma_f32_16x16x32_bf16 v[40:43], v[80:83], v[96:99], v[40:43]
	v_mfma_f32_16x16x32_bf16 v[20:23], v[88:91], v[96:99], v[20:23]
	v_mfma_f32_16x16x32_bf16 v[28:31], v[80:83], v[104:107], v[28:31]
	v_mfma_f32_16x16x32_bf16 v[12:15], v[88:91], v[104:107], v[12:15]
	v_mfma_f32_16x16x32_bf16 v[16:19], v[80:83], v[112:115], v[16:19]
	v_mfma_f32_16x16x32_bf16 v[4:7], v[88:91], v[112:115], v[4:7]
	v_mfma_f32_16x16x32_bf16 v[8:11], v[80:83], v[120:123], v[8:11]
	v_mfma_f32_16x16x32_bf16 v[0:3], v[88:91], v[120:123], v[0:3]
	v_mfma_f32_16x16x32_bf16 v[40:43], v[84:87], v[100:103], v[40:43]
	v_mfma_f32_16x16x32_bf16 v[20:23], v[92:95], v[100:103], v[20:23]
	v_mfma_f32_16x16x32_bf16 v[28:31], v[84:87], v[108:111], v[28:31]
	v_mfma_f32_16x16x32_bf16 v[12:15], v[92:95], v[108:111], v[12:15]
	v_mfma_f32_16x16x32_bf16 v[16:19], v[84:87], v[116:119], v[16:19]
	v_mfma_f32_16x16x32_bf16 v[4:7], v[92:95], v[116:119], v[4:7]
	v_mfma_f32_16x16x32_bf16 v[8:11], v[84:87], v[124:127], v[8:11]
	v_mfma_f32_16x16x32_bf16 v[0:3], v[92:95], v[124:127], v[0:3]
	s_barrier
	s_setprio 0
	s_add_u32 s42, s14, 0x80000
	s_addc_u32 s43, s15, 0
	s_mov_b32 m0, s26
	v_lshl_add_u64 v[80:81], s[42:43], 0, v[168:169]
	global_load_lds_dwordx4 v[80:81], off
	v_lshl_add_u64 v[80:81], s[42:43], 0, v[64:65]
	s_mov_b32 m0, s27
	s_nop 0
	global_load_lds_dwordx4 v[80:81], off
	s_waitcnt vmcnt(6)
	s_barrier
	s_setprio 1
	s_setprio 0
	s_add_i32 s42, 0, 0x18000
	v_add_u32_e32 v79, s42, v77
	s_barrier
	ds_read_b128 v[80:83], v79
	ds_read_b128 v[84:87], v79 offset:1024
	ds_read_b128 v[88:91], v79 offset:2048
	ds_read_b128 v[92:95], v79 offset:3072
	s_mov_b32 m0, s28
	v_lshl_add_u64 v[136:137], s[16:17], 0, v[68:69]
	ds_read_b128 v[96:99], v78 offset:32768
	ds_read_b128 v[100:103], v78 offset:33792
	ds_read_b128 v[104:107], v78 offset:34816
	ds_read_b128 v[108:111], v78 offset:35840
	ds_read_b128 v[112:115], v78 offset:36864
	ds_read_b128 v[116:119], v78 offset:37888
	ds_read_b128 v[120:123], v78 offset:38912
	ds_read_b128 v[124:127], v78 offset:39936
	global_load_lds_dwordx4 v[136:137], off
	v_lshl_add_u64 v[136:137], s[16:17], 0, v[66:67]
	s_mov_b32 m0, s29
	s_nop 0
	global_load_lds_dwordx4 v[136:137], off
	s_waitcnt lgkmcnt(8)
	s_setprio 1
	s_barrier
	s_waitcnt lgkmcnt(0)
	v_mfma_f32_16x16x32_bf16 v[60:63], v[80:83], v[96:99], v[60:63]
	v_mfma_f32_16x16x32_bf16 v[44:47], v[88:91], v[96:99], v[44:47]
	v_mfma_f32_16x16x32_bf16 v[56:59], v[80:83], v[104:107], v[56:59]
	v_mfma_f32_16x16x32_bf16 v[36:39], v[88:91], v[104:107], v[36:39]
	v_mfma_f32_16x16x32_bf16 v[52:55], v[80:83], v[112:115], v[52:55]
	v_mfma_f32_16x16x32_bf16 v[32:35], v[88:91], v[112:115], v[32:35]
	v_mfma_f32_16x16x32_bf16 v[48:51], v[80:83], v[120:123], v[48:51]
	v_mfma_f32_16x16x32_bf16 v[24:27], v[88:91], v[120:123], v[24:27]
	v_mfma_f32_16x16x32_bf16 v[60:63], v[84:87], v[100:103], v[60:63]
	v_mfma_f32_16x16x32_bf16 v[44:47], v[92:95], v[100:103], v[44:47]
	v_mfma_f32_16x16x32_bf16 v[56:59], v[84:87], v[108:111], v[56:59]
	v_mfma_f32_16x16x32_bf16 v[36:39], v[92:95], v[108:111], v[36:39]
	v_mfma_f32_16x16x32_bf16 v[52:55], v[84:87], v[116:119], v[52:55]
	v_mfma_f32_16x16x32_bf16 v[32:35], v[92:95], v[116:119], v[32:35]
	v_mfma_f32_16x16x32_bf16 v[48:51], v[84:87], v[124:127], v[48:51]
	v_mfma_f32_16x16x32_bf16 v[24:27], v[92:95], v[124:127], v[24:27]
	s_barrier
	s_setprio 0
	s_add_i32 s16, s42, s23
	v_lshl_add_u64 v[96:97], v[128:129], 0, s[94:95]
	s_mov_b32 m0, s16
	s_nop 0
	global_load_lds_dwordx4 v[96:97], off
	v_lshl_add_u64 v[96:97], v[130:131], 0, s[94:95]
	s_add_i32 m0, s16, 0x2000
	s_nop 0
	global_load_lds_dwordx4 v[96:97], off
	s_barrier
	s_waitcnt lgkmcnt(0)
	s_setprio 1
	s_setprio 0
	s_mov_b32 m0, s30
	v_lshl_add_u64 v[128:129], v[132:133], 0, s[94:95]
	s_barrier
	ds_read_b128 v[96:99], v78 offset:49152
	ds_read_b128 v[100:103], v78 offset:50176
	ds_read_b128 v[104:107], v78 offset:51200
	ds_read_b128 v[108:111], v78 offset:52224
	ds_read_b128 v[112:115], v78 offset:53248
	ds_read_b128 v[116:119], v78 offset:54272
	ds_read_b128 v[120:123], v78 offset:55296
	ds_read_b128 v[124:127], v78 offset:56320
	global_load_lds_dwordx4 v[128:129], off
	v_lshl_add_u64 v[128:129], v[134:135], 0, s[94:95]
	s_mov_b32 m0, s31
	s_nop 0
	global_load_lds_dwordx4 v[128:129], off
	s_setprio 1
	s_barrier
	s_waitcnt lgkmcnt(0)
	v_mfma_f32_16x16x32_bf16 v[40:43], v[80:83], v[96:99], v[40:43]
	v_mfma_f32_16x16x32_bf16 v[20:23], v[88:91], v[96:99], v[20:23]
	v_mfma_f32_16x16x32_bf16 v[28:31], v[80:83], v[104:107], v[28:31]
	v_mfma_f32_16x16x32_bf16 v[12:15], v[88:91], v[104:107], v[12:15]
	v_mfma_f32_16x16x32_bf16 v[16:19], v[80:83], v[112:115], v[16:19]
	v_mfma_f32_16x16x32_bf16 v[4:7], v[88:91], v[112:115], v[4:7]
	v_mfma_f32_16x16x32_bf16 v[8:11], v[80:83], v[120:123], v[8:11]
	v_mfma_f32_16x16x32_bf16 v[0:3], v[88:91], v[120:123], v[0:3]
	v_mfma_f32_16x16x32_bf16 v[40:43], v[84:87], v[100:103], v[40:43]
	v_mfma_f32_16x16x32_bf16 v[20:23], v[92:95], v[100:103], v[20:23]
	v_mfma_f32_16x16x32_bf16 v[28:31], v[84:87], v[108:111], v[28:31]
	v_mfma_f32_16x16x32_bf16 v[12:15], v[92:95], v[108:111], v[12:15]
	v_mfma_f32_16x16x32_bf16 v[16:19], v[84:87], v[116:119], v[16:19]
	v_mfma_f32_16x16x32_bf16 v[4:7], v[92:95], v[116:119], v[4:7]
	v_mfma_f32_16x16x32_bf16 v[8:11], v[84:87], v[124:127], v[8:11]
	v_mfma_f32_16x16x32_bf16 v[0:3], v[92:95], v[124:127], v[0:3]
	s_barrier
	s_setprio 0
	s_add_u32 s14, s14, 0x80080
	s_addc_u32 s15, s15, 0
	s_mov_b32 m0, s34
	v_lshl_add_u64 v[80:81], s[14:15], 0, v[168:169]
	global_load_lds_dwordx4 v[80:81], off
	v_lshl_add_u64 v[80:81], s[14:15], 0, v[64:65]
	s_mov_b32 m0, s35
	s_nop 0
	global_load_lds_dwordx4 v[80:81], off
	s_waitcnt vmcnt(6)
	s_barrier
	s_setprio 1
	s_setprio 0
	s_add_i32 s41, s41, 2
	s_add_u32 s12, s12, 0x100
	s_addc_u32 s13, s13, 0
	s_add_u32 s39, s39, 0x100
	s_addc_u32 s40, s40, 0
	s_cmp_gt_u32 s41, 13
	s_barrier
	s_cbranch_scc0 .LBB0_440
	s_and_b64 vcc, exec, s[2:3]
	s_cbranch_vccz .LBB0_444
	s_barrier
	s_andn2_b64 vcc, exec, s[4:5]
	s_cbranch_vccnz .LBB0_445

.LBB0_1191:
	s_add_u32 s12, s10, 0x80
	s_addc_u32 s13, s11, 0
	s_add_i32 s40, 0, 0x10000
	v_add_u32_e32 v79, s40, v77
	ds_read_b128 v[80:83], v79
	ds_read_b128 v[84:87], v79 offset:1024
	ds_read_b128 v[88:91], v79 offset:2048
	ds_read_b128 v[92:95], v79 offset:3072
	s_cmp_eq_u32 s39, 4
	s_cselect_b32 s15, s5, s13
	s_cselect_b32 s14, s4, s12
	s_cselect_b32 s13, s7, s38
	s_cselect_b32 s12, s6, s37
	v_lshl_add_u64 v[128:129], s[10:11], 0, v[74:75]
	s_add_i32 m0, s22, 0xc000
	ds_read_b128 v[96:99], v78
	ds_read_b128 v[100:103], v78 offset:1024
	ds_read_b128 v[104:107], v78 offset:2048
	ds_read_b128 v[108:111], v78 offset:3072
	ds_read_b128 v[112:115], v78 offset:4096
	ds_read_b128 v[116:119], v78 offset:5120
	ds_read_b128 v[120:123], v78 offset:6144
	ds_read_b128 v[124:127], v78 offset:7168
	global_load_lds_dwordx4 v[128:129], off
	v_lshl_add_u64 v[128:129], s[10:11], 0, v[72:73]
	s_add_i32 m0, s22, 0xe000
	s_nop 0
	global_load_lds_dwordx4 v[128:129], off
	s_waitcnt lgkmcnt(8)
	s_setprio 1
	s_barrier
	s_waitcnt lgkmcnt(0)
	v_mfma_f32_16x16x32_bf16 v[60:63], v[80:83], v[96:99], v[60:63]
	v_mfma_f32_16x16x32_bf16 v[44:47], v[88:91], v[96:99], v[44:47]
	v_mfma_f32_16x16x32_bf16 v[56:59], v[80:83], v[104:107], v[56:59]
	v_mfma_f32_16x16x32_bf16 v[36:39], v[88:91], v[104:107], v[36:39]
	v_mfma_f32_16x16x32_bf16 v[52:55], v[80:83], v[112:115], v[52:55]
	v_mfma_f32_16x16x32_bf16 v[32:35], v[88:91], v[112:115], v[32:35]
	v_mfma_f32_16x16x32_bf16 v[48:51], v[80:83], v[120:123], v[48:51]
	v_mfma_f32_16x16x32_bf16 v[24:27], v[88:91], v[120:123], v[24:27]
	v_mfma_f32_16x16x32_bf16 v[60:63], v[84:87], v[100:103], v[60:63]
	v_mfma_f32_16x16x32_bf16 v[44:47], v[92:95], v[100:103], v[44:47]
	v_mfma_f32_16x16x32_bf16 v[56:59], v[84:87], v[108:111], v[56:59]
	v_mfma_f32_16x16x32_bf16 v[36:39], v[92:95], v[108:111], v[36:39]
	v_mfma_f32_16x16x32_bf16 v[52:55], v[84:87], v[116:119], v[52:55]
	v_mfma_f32_16x16x32_bf16 v[32:35], v[92:95], v[116:119], v[32:35]
	v_mfma_f32_16x16x32_bf16 v[48:51], v[84:87], v[124:127], v[48:51]
	v_mfma_f32_16x16x32_bf16 v[24:27], v[92:95], v[124:127], v[24:27]
	s_barrier
	s_setprio 0
	s_add_i32 s40, s40, s21
	v_lshl_add_u64 v[128:129], s[12:13], 0, v[168:169]
	s_mov_b32 m0, s40
	v_lshl_add_u64 v[130:131], s[12:13], 0, v[64:65]
	global_load_lds_dwordx4 v[128:129], off
	s_add_i32 m0, s40, 0x2000
	s_nop 0
	global_load_lds_dwordx4 v[130:131], off
	s_barrier
	s_waitcnt lgkmcnt(0)
	s_setprio 1
	s_setprio 0
	s_mov_b32 m0, s22
	v_lshl_add_u64 v[132:133], s[14:15], 0, v[168:169]
	s_barrier
	ds_read_b128 v[96:99], v78 offset:16384
	ds_read_b128 v[100:103], v78 offset:17408
	ds_read_b128 v[104:107], v78 offset:18432
	ds_read_b128 v[108:111], v78 offset:19456
	ds_read_b128 v[112:115], v78 offset:20480
	ds_read_b128 v[116:119], v78 offset:21504
	ds_read_b128 v[120:123], v78 offset:22528
	ds_read_b128 v[124:127], v78 offset:23552
	global_load_lds_dwordx4 v[132:133], off
	v_lshl_add_u64 v[134:135], s[14:15], 0, v[64:65]
	s_mov_b32 m0, s23
	s_nop 0
	global_load_lds_dwordx4 v[134:135], off
	s_setprio 1
	s_barrier
	s_waitcnt lgkmcnt(0)
	v_mfma_f32_16x16x32_bf16 v[40:43], v[80:83], v[96:99], v[40:43]
	v_mfma_f32_16x16x32_bf16 v[20:23], v[88:91], v[96:99], v[20:23]
	v_mfma_f32_16x16x32_bf16 v[28:31], v[80:83], v[104:107], v[28:31]
	v_mfma_f32_16x16x32_bf16 v[12:15], v[88:91], v[104:107], v[12:15]
	v_mfma_f32_16x16x32_bf16 v[16:19], v[80:83], v[112:115], v[16:19]
	v_mfma_f32_16x16x32_bf16 v[4:7], v[88:91], v[112:115], v[4:7]
	v_mfma_f32_16x16x32_bf16 v[8:11], v[80:83], v[120:123], v[8:11]
	v_mfma_f32_16x16x32_bf16 v[0:3], v[88:91], v[120:123], v[0:3]
	v_mfma_f32_16x16x32_bf16 v[40:43], v[84:87], v[100:103], v[40:43]
	v_mfma_f32_16x16x32_bf16 v[20:23], v[92:95], v[100:103], v[20:23]
	v_mfma_f32_16x16x32_bf16 v[28:31], v[84:87], v[108:111], v[28:31]
	v_mfma_f32_16x16x32_bf16 v[12:15], v[92:95], v[108:111], v[12:15]
	v_mfma_f32_16x16x32_bf16 v[16:19], v[84:87], v[116:119], v[16:19]
	v_mfma_f32_16x16x32_bf16 v[4:7], v[92:95], v[116:119], v[4:7]
	v_mfma_f32_16x16x32_bf16 v[8:11], v[84:87], v[124:127], v[8:11]
	v_mfma_f32_16x16x32_bf16 v[0:3], v[92:95], v[124:127], v[0:3]
	s_barrier
	s_setprio 0
	s_add_u32 s40, s12, 0x80000
	s_addc_u32 s41, s13, 0
	s_mov_b32 m0, s24
	v_lshl_add_u64 v[80:81], s[40:41], 0, v[168:169]
	global_load_lds_dwordx4 v[80:81], off
	v_lshl_add_u64 v[80:81], s[40:41], 0, v[64:65]
	s_mov_b32 m0, s25
	s_nop 0
	global_load_lds_dwordx4 v[80:81], off
	s_waitcnt vmcnt(6)
	s_barrier
	s_setprio 1
	s_setprio 0
	s_add_i32 s40, 0, 0x18000
	v_add_u32_e32 v79, s40, v77
	s_barrier
	ds_read_b128 v[80:83], v79
	ds_read_b128 v[84:87], v79 offset:1024
	ds_read_b128 v[88:91], v79 offset:2048
	ds_read_b128 v[92:95], v79 offset:3072
	s_mov_b32 m0, s26
	v_lshl_add_u64 v[136:137], s[14:15], 0, v[68:69]
	ds_read_b128 v[96:99], v78 offset:32768
	ds_read_b128 v[100:103], v78 offset:33792
	ds_read_b128 v[104:107], v78 offset:34816
	ds_read_b128 v[108:111], v78 offset:35840
	ds_read_b128 v[112:115], v78 offset:36864
	ds_read_b128 v[116:119], v78 offset:37888
	ds_read_b128 v[120:123], v78 offset:38912
	ds_read_b128 v[124:127], v78 offset:39936
	global_load_lds_dwordx4 v[136:137], off
	v_lshl_add_u64 v[136:137], s[14:15], 0, v[66:67]
	s_mov_b32 m0, s27
	s_nop 0
	global_load_lds_dwordx4 v[136:137], off
	s_waitcnt lgkmcnt(8)
	s_setprio 1
	s_barrier
	s_waitcnt lgkmcnt(0)
	v_mfma_f32_16x16x32_bf16 v[60:63], v[80:83], v[96:99], v[60:63]
	v_mfma_f32_16x16x32_bf16 v[44:47], v[88:91], v[96:99], v[44:47]
	v_mfma_f32_16x16x32_bf16 v[56:59], v[80:83], v[104:107], v[56:59]
	v_mfma_f32_16x16x32_bf16 v[36:39], v[88:91], v[104:107], v[36:39]
	v_mfma_f32_16x16x32_bf16 v[52:55], v[80:83], v[112:115], v[52:55]
	v_mfma_f32_16x16x32_bf16 v[32:35], v[88:91], v[112:115], v[32:35]
	v_mfma_f32_16x16x32_bf16 v[48:51], v[80:83], v[120:123], v[48:51]
	v_mfma_f32_16x16x32_bf16 v[24:27], v[88:91], v[120:123], v[24:27]
	v_mfma_f32_16x16x32_bf16 v[60:63], v[84:87], v[100:103], v[60:63]
	v_mfma_f32_16x16x32_bf16 v[44:47], v[92:95], v[100:103], v[44:47]
	v_mfma_f32_16x16x32_bf16 v[56:59], v[84:87], v[108:111], v[56:59]
	v_mfma_f32_16x16x32_bf16 v[36:39], v[92:95], v[108:111], v[36:39]
	v_mfma_f32_16x16x32_bf16 v[52:55], v[84:87], v[116:119], v[52:55]
	v_mfma_f32_16x16x32_bf16 v[32:35], v[92:95], v[116:119], v[32:35]
	v_mfma_f32_16x16x32_bf16 v[48:51], v[84:87], v[124:127], v[48:51]
	v_mfma_f32_16x16x32_bf16 v[24:27], v[92:95], v[124:127], v[24:27]
	s_barrier
	s_setprio 0
	s_add_i32 s14, s40, s21
	v_lshl_add_u64 v[96:97], v[128:129], 0, s[94:95]
	s_mov_b32 m0, s14
	s_nop 0
	global_load_lds_dwordx4 v[96:97], off
	v_lshl_add_u64 v[96:97], v[130:131], 0, s[94:95]
	s_add_i32 m0, s14, 0x2000
	s_nop 0
	global_load_lds_dwordx4 v[96:97], off
	s_barrier
	s_waitcnt lgkmcnt(0)
	s_setprio 1
	s_setprio 0
	s_mov_b32 m0, s28
	v_lshl_add_u64 v[128:129], v[132:133], 0, s[94:95]
	s_barrier
	ds_read_b128 v[96:99], v78 offset:49152
	ds_read_b128 v[100:103], v78 offset:50176
	ds_read_b128 v[104:107], v78 offset:51200
	ds_read_b128 v[108:111], v78 offset:52224
	ds_read_b128 v[112:115], v78 offset:53248
	ds_read_b128 v[116:119], v78 offset:54272
	ds_read_b128 v[120:123], v78 offset:55296
	ds_read_b128 v[124:127], v78 offset:56320
	global_load_lds_dwordx4 v[128:129], off
	v_lshl_add_u64 v[128:129], v[134:135], 0, s[94:95]
	s_mov_b32 m0, s29
	s_nop 0
	global_load_lds_dwordx4 v[128:129], off
	s_setprio 1
	s_barrier
	s_waitcnt lgkmcnt(0)
	v_mfma_f32_16x16x32_bf16 v[40:43], v[80:83], v[96:99], v[40:43]
	v_mfma_f32_16x16x32_bf16 v[20:23], v[88:91], v[96:99], v[20:23]
	v_mfma_f32_16x16x32_bf16 v[28:31], v[80:83], v[104:107], v[28:31]
	v_mfma_f32_16x16x32_bf16 v[12:15], v[88:91], v[104:107], v[12:15]
	v_mfma_f32_16x16x32_bf16 v[16:19], v[80:83], v[112:115], v[16:19]
	v_mfma_f32_16x16x32_bf16 v[4:7], v[88:91], v[112:115], v[4:7]
	v_mfma_f32_16x16x32_bf16 v[8:11], v[80:83], v[120:123], v[8:11]
	v_mfma_f32_16x16x32_bf16 v[0:3], v[88:91], v[120:123], v[0:3]
	v_mfma_f32_16x16x32_bf16 v[40:43], v[84:87], v[100:103], v[40:43]
	v_mfma_f32_16x16x32_bf16 v[20:23], v[92:95], v[100:103], v[20:23]
	v_mfma_f32_16x16x32_bf16 v[28:31], v[84:87], v[108:111], v[28:31]
	v_mfma_f32_16x16x32_bf16 v[12:15], v[92:95], v[108:111], v[12:15]
	v_mfma_f32_16x16x32_bf16 v[16:19], v[84:87], v[116:119], v[16:19]
	v_mfma_f32_16x16x32_bf16 v[4:7], v[92:95], v[116:119], v[4:7]
	v_mfma_f32_16x16x32_bf16 v[8:11], v[84:87], v[124:127], v[8:11]
	v_mfma_f32_16x16x32_bf16 v[0:3], v[92:95], v[124:127], v[0:3]
	s_barrier
	s_setprio 0
	s_add_u32 s12, s12, 0x80080
	s_addc_u32 s13, s13, 0
	s_mov_b32 m0, s30
	v_lshl_add_u64 v[80:81], s[12:13], 0, v[168:169]
	global_load_lds_dwordx4 v[80:81], off
	v_lshl_add_u64 v[80:81], s[12:13], 0, v[64:65]
	s_mov_b32 m0, s31
	s_nop 0
	global_load_lds_dwordx4 v[80:81], off
	s_waitcnt vmcnt(6)
	s_barrier
	s_setprio 1
	s_setprio 0
	s_add_i32 s39, s39, 2
	s_add_u32 s10, s10, 0x100
	s_addc_u32 s11, s11, 0
	s_add_u32 s37, s37, 0x100
	s_addc_u32 s38, s38, 0
	s_cmp_gt_u32 s39, 5
	s_barrier
	s_cbranch_scc0 .LBB0_1191
	s_and_b64 vcc, exec, s[2:3]
	s_cbranch_vccz .LBB0_1194
	s_barrier
